# grouped GEMM unit decode (gate/up, down, both layers): scalar shift/mask fast path when the group height is 8, generic divide kept for the tail group; on top of the SwiGLU reciprocal merge
# speedup vs baseline: 1.0014x; 1.0004x over previous
.LBB0_1538:
	v_cmp_ge_i64_e32 vcc, s[38:39], v[144:145]
	v_cmp_lt_i64_e64 s[8:9], s[38:39], v[144:145]
	s_cbranch_vccnz .LBB0_1540
	s_ashr_i32 s6, s38, 31
	s_lshr_b32 s6, s6, 29
	s_add_i32 s6, s38, s6
	s_ashr_i32 s7, s6, 3
	s_and_b32 s6, s6, -8
	s_sub_i32 s6, s38, s6
	s_cmp_lt_i32 s6, 0
	s_cselect_b32 s68, s56, s0
	s_mul_i32 s6, s68, s6
	s_add_i32 s6, s6, s7
	s_ashr_i32 s7, s6, 31
	s_lshr_b32 s7, s7, 26
	s_add_i32 s7, s6, s7
	s_ashr_i32 s68, s7, 6
	s_lshl_b32 s69, s68, 3
	s_sub_i32 s68, s0, s69
	s_min_i32 s71, s68, 8
	s_cmp_eq_u32 s71, 8
	s_cbranch_scc0 .Ldecs_gu0
	s_andn2_b32 s7, s7, 63
	s_sub_i32 s6, s6, s7
	s_lshr_b32 s68, s6, 3
	s_and_b32 s6, s6, 7
	s_branch .Ldecj_gu0
.Ldecs_gu0:
	s_abs_i32 s68, s71
	v_cvt_f32_u32_e32 v2, s68
	s_sub_i32 s73, 0, s68
	s_andn2_b32 s7, s7, 63
	s_sub_i32 s6, s6, s7
	v_rcp_iflag_f32_e32 v2, v2
	s_abs_i32 s7, s6
	s_xor_b32 s72, s6, s71
	s_ashr_i32 s72, s72, 31
	v_mul_f32_e32 v2, 0x4f7ffffe, v2
	v_cvt_u32_f32_e32 v2, v2
	s_nop 0
	v_readfirstlane_b32 s74, v2
	s_mul_i32 s73, s73, s74
	s_mul_hi_u32 s73, s74, s73
	s_add_i32 s74, s74, s73
	s_mul_hi_u32 s73, s7, s74
	s_mul_i32 s74, s73, s68
	s_sub_i32 s7, s7, s74
	s_add_i32 s75, s73, 1
	s_sub_i32 s74, s7, s68
	s_cmp_ge_u32 s7, s68
	s_cselect_b32 s73, s75, s73
	s_cselect_b32 s7, s74, s7
	s_add_i32 s74, s73, 1
	s_cmp_ge_u32 s7, s68
	s_cselect_b32 s7, s74, s73
	s_xor_b32 s7, s7, s72
	s_sub_i32 s68, s7, s72
	s_mul_i32 s7, s68, s71
	s_sub_i32 s6, s6, s7
.Ldecj_gu0:
	s_add_i32 s72, s6, s69
	s_add_i32 s6, s72, 0
	s_add_i32 s6, s6, 0x25d00
	v_mov_b32_e32 v2, s6
	ds_read_u8 v2, v2
	s_waitcnt lgkmcnt(0)
	v_readfirstlane_b32 s74, v2

.LBB0_1622:
	s_ashr_i32 s8, s38, 3
	s_add_i32 s8, s40, s8
	s_ashr_i32 s9, s8, 31
	s_lshr_b32 s9, s9, 27
	s_add_i32 s9, s8, s9
	s_ashr_i32 s38, s9, 5
	s_lshl_b32 s39, s38, 3
	s_sub_i32 s38, s0, s39
	s_min_i32 s40, s38, 8
	s_cmp_eq_u32 s40, 8
	s_cbranch_scc0 .Ldecs_dn0
	s_andn2_b32 s9, s9, 31
	s_sub_i32 s8, s8, s9
	s_lshr_b32 s38, s8, 3
	s_and_b32 s8, s8, 7
	s_branch .Ldecj_dn0
.Ldecs_dn0:
	s_abs_i32 s38, s40
	v_cvt_f32_u32_e32 v10, s38
	s_sub_i32 s42, 0, s38
	s_andn2_b32 s9, s9, 31
	s_sub_i32 s8, s8, s9
	v_rcp_iflag_f32_e32 v10, v10
	s_abs_i32 s9, s8
	s_xor_b32 s41, s8, s40
	s_ashr_i32 s41, s41, 31
	v_mul_f32_e32 v10, 0x4f7ffffe, v10
	v_cvt_u32_f32_e32 v10, v10
	s_nop 0
	v_readfirstlane_b32 s43, v10
	s_mul_i32 s42, s42, s43
	s_mul_hi_u32 s42, s43, s42
	s_add_i32 s43, s43, s42
	s_mul_hi_u32 s42, s9, s43
	s_mul_i32 s43, s42, s38
	s_sub_i32 s9, s9, s43
	s_add_i32 s44, s42, 1
	s_sub_i32 s43, s9, s38
	s_cmp_ge_u32 s9, s38
	s_cselect_b32 s42, s44, s42
	s_cselect_b32 s9, s43, s9
	s_add_i32 s43, s42, 1
	s_cmp_ge_u32 s9, s38
	s_cselect_b32 s9, s43, s42
	s_xor_b32 s9, s9, s41
	s_sub_i32 s38, s9, s41
	s_mul_i32 s9, s38, s40
	s_sub_i32 s8, s8, s9
.Ldecj_dn0:
	s_add_i32 s40, s39, s8
	s_add_i32 s8, s40, 0
	s_add_i32 s8, s8, 0x25d00
	v_mov_b32_e32 v10, s8
	ds_read_u8 v10, v10
	s_waitcnt lgkmcnt(0)
	v_readfirstlane_b32 s42, v10

.LBB0_3340:
	v_cmp_ge_i64_e32 vcc, s[40:41], v[144:145]
	v_cmp_lt_i64_e64 s[10:11], s[40:41], v[144:145]
	s_cbranch_vccnz .LBB0_3342
	s_ashr_i32 s8, s40, 31
	s_lshr_b32 s8, s8, 29
	s_add_i32 s8, s40, s8
	s_ashr_i32 s9, s8, 3
	s_and_b32 s8, s8, -8
	s_sub_i32 s8, s40, s8
	s_cmp_lt_i32 s8, 0
	s_cselect_b32 s64, s54, s0
	s_mul_i32 s8, s64, s8
	s_add_i32 s8, s8, s9
	s_ashr_i32 s9, s8, 31
	s_lshr_b32 s9, s9, 26
	s_add_i32 s9, s8, s9
	s_ashr_i32 s64, s9, 6
	s_lshl_b32 s65, s64, 3
	s_sub_i32 s64, s0, s65
	s_min_i32 s66, s64, 8
	s_cmp_eq_u32 s66, 8
	s_cbranch_scc0 .Ldecs_gu1
	s_andn2_b32 s9, s9, 63
	s_sub_i32 s8, s8, s9
	s_lshr_b32 s64, s8, 3
	s_and_b32 s8, s8, 7
	s_branch .Ldecj_gu1
.Ldecs_gu1:
	s_abs_i32 s64, s66
	v_cvt_f32_u32_e32 v2, s64
	s_sub_i32 s68, 0, s64
	s_andn2_b32 s9, s9, 63
	s_sub_i32 s8, s8, s9
	v_rcp_iflag_f32_e32 v2, v2
	s_abs_i32 s9, s8
	s_xor_b32 s67, s8, s66
	s_ashr_i32 s67, s67, 31
	v_mul_f32_e32 v2, 0x4f7ffffe, v2
	v_cvt_u32_f32_e32 v2, v2
	s_nop 0
	v_readfirstlane_b32 s70, v2
	s_mul_i32 s68, s68, s70
	s_mul_hi_u32 s68, s70, s68
	s_add_i32 s70, s70, s68
	s_mul_hi_u32 s68, s9, s70
	s_mul_i32 s70, s68, s64
	s_sub_i32 s9, s9, s70
	s_add_i32 s71, s68, 1
	s_sub_i32 s70, s9, s64
	s_cmp_ge_u32 s9, s64
	s_cselect_b32 s68, s71, s68
	s_cselect_b32 s9, s70, s9
	s_add_i32 s70, s68, 1
	s_cmp_ge_u32 s9, s64
	s_cselect_b32 s9, s70, s68
	s_xor_b32 s9, s9, s67
	s_sub_i32 s64, s9, s67
	s_mul_i32 s9, s64, s66
	s_sub_i32 s8, s8, s9
.Ldecj_gu1:
	s_add_i32 s66, s8, s65
	s_add_i32 s8, s66, 0
	s_add_i32 s8, s8, 0x25d00
	v_mov_b32_e32 v2, s8
	ds_read_u8 v2, v2
	s_waitcnt lgkmcnt(0)
	v_readfirstlane_b32 s70, v2

.LBB0_3424:
	s_ashr_i32 s10, s40, 3
	s_add_i32 s10, s42, s10
	s_ashr_i32 s11, s10, 31
	s_lshr_b32 s11, s11, 27
	s_add_i32 s11, s10, s11
	s_ashr_i32 s40, s11, 5
	s_lshl_b32 s41, s40, 3
	s_sub_i32 s40, s0, s41
	s_min_i32 s42, s40, 8
	s_cmp_eq_u32 s42, 8
	s_cbranch_scc0 .Ldecs_dn1
	s_andn2_b32 s11, s11, 31
	s_sub_i32 s10, s10, s11
	s_lshr_b32 s40, s10, 3
	s_and_b32 s10, s10, 7
	s_branch .Ldecj_dn1
.Ldecs_dn1:
	s_abs_i32 s40, s42
	v_cvt_f32_u32_e32 v10, s40
	s_sub_i32 s44, 0, s40
	s_andn2_b32 s11, s11, 31
	s_sub_i32 s10, s10, s11
	v_rcp_iflag_f32_e32 v10, v10
	s_abs_i32 s11, s10
	s_xor_b32 s43, s10, s42
	s_ashr_i32 s43, s43, 31
	v_mul_f32_e32 v10, 0x4f7ffffe, v10
	v_cvt_u32_f32_e32 v10, v10
	s_nop 0
	v_readfirstlane_b32 s45, v10
	s_mul_i32 s44, s44, s45
	s_mul_hi_u32 s44, s45, s44
	s_add_i32 s45, s45, s44
	s_mul_hi_u32 s44, s11, s45
	s_mul_i32 s45, s44, s40
	s_sub_i32 s11, s11, s45
	s_add_i32 s46, s44, 1
	s_sub_i32 s45, s11, s40
	s_cmp_ge_u32 s11, s40
	s_cselect_b32 s44, s46, s44
	s_cselect_b32 s11, s45, s11
	s_add_i32 s45, s44, 1
	s_cmp_ge_u32 s11, s40
	s_cselect_b32 s11, s45, s44
	s_xor_b32 s11, s11, s43
	s_sub_i32 s40, s11, s43
	s_mul_i32 s11, s40, s42
	s_sub_i32 s10, s10, s11
.Ldecj_dn1:
	s_add_i32 s42, s41, s10
	s_add_i32 s10, s42, 0
	s_add_i32 s10, s10, 0x25d00
	v_mov_b32_e32 v10, s10
	ds_read_u8 v10, v10
	s_waitcnt lgkmcnt(0)
	v_readfirstlane_b32 s44, v10
